# baseline (speedup 1.0000x reference)
.LBB0_9:
	s_or_b64 exec, exec, s[4:5]
	v_add_u32_e32 v46, 0x100, v46
	v_cmp_lt_u32_e64 s[2:3], 39, v46
	global_store_dwordx4 v[42:43], v[34:37], off sc1
	v_lshl_add_u64 v[42:43], v[42:43], 0, s[10:11]
	s_or_b64 s[8:9], s[2:3], s[8:9]
	v_add_u32_e32 v47, 32, v47
	s_andn2_b64 exec, exec, s[8:9]
	s_cbranch_execz .LBB0_32

.LBB0_46:
	s_or_b64 exec, exec, s[4:5]
	v_lshlrev_b32_e32 v2, 5, v44
	s_waitcnt lgkmcnt(0)
	s_barrier
	ds_read_b128 v[14:17], v2 offset:20480
	ds_read_b128 v[2:5], v2 offset:20496
	v_mov_b32_e32 v41, 0
	v_lshlrev_b32_e32 v40, 4, v1
	s_waitcnt lgkmcnt(1)
	v_cmp_gt_i32_e64 s[16:17], 0, v14
	v_max_i32_e32 v42, 0, v14
	v_lshl_add_u32 v42, v42, 10, v40
	global_load_dwordx4 v[48:51], v42, s[24:25] nt
	v_cmp_gt_i32_e64 s[14:15], 0, v15
	v_max_i32_e32 v43, 0, v15
	v_lshl_add_u32 v43, v43, 10, v40
	global_load_dwordx4 v[34:37], v43, s[24:25] nt
	v_cmp_gt_i32_e64 s[12:13], 0, v16
	v_max_i32_e32 v42, 0, v16
	v_lshl_add_u32 v42, v42, 10, v40
	global_load_dwordx4 v[30:33], v42, s[24:25] nt
	v_cmp_gt_i32_e64 s[10:11], 0, v17
	v_max_i32_e32 v43, 0, v17
	v_lshl_add_u32 v43, v43, 10, v40
	global_load_dwordx4 v[26:29], v43, s[24:25] nt
	s_waitcnt lgkmcnt(0)
	v_cmp_gt_i32_e64 s[8:9], 0, v2
	v_max_i32_e32 v42, 0, v2
	v_lshl_add_u32 v42, v42, 10, v40
	global_load_dwordx4 v[22:25], v42, s[24:25] nt
	v_cmp_gt_i32_e64 s[6:7], 0, v3
	v_max_i32_e32 v43, 0, v3
	v_lshl_add_u32 v43, v43, 10, v40
	global_load_dwordx4 v[18:21], v43, s[24:25] nt
	v_cmp_gt_i32_e64 s[4:5], 0, v4
	v_max_i32_e32 v42, 0, v4
	v_lshl_add_u32 v42, v42, 10, v40
	global_load_dwordx4 v[10:13], v42, s[24:25] nt
	v_cmp_gt_i32_e64 s[2:3], 0, v5
	v_max_i32_e32 v43, 0, v5
	v_lshl_add_u32 v43, v43, 10, v40
	global_load_dwordx4 v[6:9], v43, s[24:25] nt
	v_lshlrev_b32_e32 v1, 8, v0
	v_lshlrev_b32_e32 v0, 3, v0
	s_movk_i32 s19, 0x3c00
	v_and_b32_e32 v0, 8, v0
	v_and_or_b32 v46, v1, s19, v0
	s_mul_i32 s18, s20, 0x4080
	s_mul_hi_u32 s24, s20, 0x4080
	s_add_u32 s18, s22, s18
	v_lshlrev_b32_e32 v39, 3, v44
	v_and_b32_e32 v41, 32, v38
	s_addc_u32 s19, s23, s24
	s_add_u32 s22, s18, 0x4000
	s_addc_u32 s23, s19, 0
	v_add_u32_e32 v60, v39, v41
	v_lshl_add_u32 v60, v60, 4, v46
	v_lshrrev_b32_e32 v67, 1, v40
	v_and_b32_e32 v67, 0x70, v67
	v_or_b32_e32 v67, v60, v67
	v_mov_b32_e32 v66, 0x7f800000
	s_waitcnt vmcnt(7)
	v_cndmask_b32_e64 v48, v48, 0, s[16:17]
	v_cndmask_b32_e64 v49, v49, 0, s[16:17]
	v_cndmask_b32_e64 v50, v50, 0, s[16:17]
	v_cndmask_b32_e64 v51, v51, 0, s[16:17]
	v_pk_mul_f32 v[62:63], v[48:49], v[48:49]
	v_pk_mul_f32 v[64:65], v[50:51], v[50:51]
	v_add_f32_e32 v52, v62, v63
	v_add_f32_e32 v52, v52, v64
	v_add_f32_e32 v52, v52, v65
	v_cvt_pk_f16_f32 v62, v48, v49
	v_cvt_pk_f16_f32 v63, v50, v51
	ds_write_b64 v67, v[62:63]
	s_waitcnt vmcnt(6)
	v_cndmask_b32_e64 v34, v34, 0, s[14:15]
	v_cndmask_b32_e64 v35, v35, 0, s[14:15]
	v_cndmask_b32_e64 v36, v36, 0, s[14:15]
	v_cndmask_b32_e64 v37, v37, 0, s[14:15]
	v_pk_mul_f32 v[62:63], v[34:35], v[34:35]
	v_pk_mul_f32 v[64:65], v[36:37], v[36:37]
	v_add_f32_e32 v53, v62, v63
	v_add_f32_e32 v53, v53, v64
	v_add_f32_e32 v53, v53, v65
	v_cvt_pk_f16_f32 v62, v34, v35
	v_cvt_pk_f16_f32 v63, v36, v37
	v_xor_b32_e32 v68, 0x10, v67
	ds_write_b64 v68, v[62:63]
	s_waitcnt vmcnt(5)
	v_cndmask_b32_e64 v30, v30, 0, s[12:13]
	v_cndmask_b32_e64 v31, v31, 0, s[12:13]
	v_cndmask_b32_e64 v32, v32, 0, s[12:13]
	v_cndmask_b32_e64 v33, v33, 0, s[12:13]
	v_pk_mul_f32 v[62:63], v[30:31], v[30:31]
	v_pk_mul_f32 v[64:65], v[32:33], v[32:33]
	v_add_f32_e32 v54, v62, v63
	v_add_f32_e32 v54, v54, v64
	v_add_f32_e32 v54, v54, v65
	v_cvt_pk_f16_f32 v62, v30, v31
	v_cvt_pk_f16_f32 v63, v32, v33
	v_xor_b32_e32 v68, 0x20, v67
	ds_write_b64 v68, v[62:63]
	s_waitcnt vmcnt(4)
	v_cndmask_b32_e64 v26, v26, 0, s[10:11]
	v_cndmask_b32_e64 v27, v27, 0, s[10:11]
	v_cndmask_b32_e64 v28, v28, 0, s[10:11]
	v_cndmask_b32_e64 v29, v29, 0, s[10:11]
	v_pk_mul_f32 v[62:63], v[26:27], v[26:27]
	v_pk_mul_f32 v[64:65], v[28:29], v[28:29]
	v_add_f32_e32 v55, v62, v63
	v_add_f32_e32 v55, v55, v64
	v_add_f32_e32 v55, v55, v65
	v_cvt_pk_f16_f32 v62, v26, v27
	v_cvt_pk_f16_f32 v63, v28, v29
	v_xor_b32_e32 v68, 0x30, v67
	ds_write_b64 v68, v[62:63]
	s_waitcnt vmcnt(3)
	v_cndmask_b32_e64 v22, v22, 0, s[8:9]
	v_cndmask_b32_e64 v23, v23, 0, s[8:9]
	v_cndmask_b32_e64 v24, v24, 0, s[8:9]
	v_cndmask_b32_e64 v25, v25, 0, s[8:9]
	v_pk_mul_f32 v[62:63], v[22:23], v[22:23]
	v_pk_mul_f32 v[64:65], v[24:25], v[24:25]
	v_add_f32_e32 v56, v62, v63
	v_add_f32_e32 v56, v56, v64
	v_add_f32_e32 v56, v56, v65
	v_cvt_pk_f16_f32 v62, v22, v23
	v_cvt_pk_f16_f32 v63, v24, v25
	v_xor_b32_e32 v68, 0x40, v67
	ds_write_b64 v68, v[62:63]
	s_waitcnt vmcnt(2)
	v_cndmask_b32_e64 v18, v18, 0, s[6:7]
	v_cndmask_b32_e64 v19, v19, 0, s[6:7]
	v_cndmask_b32_e64 v20, v20, 0, s[6:7]
	v_cndmask_b32_e64 v21, v21, 0, s[6:7]
	v_pk_mul_f32 v[62:63], v[18:19], v[18:19]
	v_pk_mul_f32 v[64:65], v[20:21], v[20:21]
	v_add_f32_e32 v57, v62, v63
	v_add_f32_e32 v57, v57, v64
	v_add_f32_e32 v57, v57, v65
	v_cvt_pk_f16_f32 v62, v18, v19
	v_cvt_pk_f16_f32 v63, v20, v21
	v_xor_b32_e32 v68, 0x50, v67
	ds_write_b64 v68, v[62:63]
	s_waitcnt vmcnt(1)
	v_cndmask_b32_e64 v10, v10, 0, s[4:5]
	v_cndmask_b32_e64 v11, v11, 0, s[4:5]
	v_cndmask_b32_e64 v12, v12, 0, s[4:5]
	v_cndmask_b32_e64 v13, v13, 0, s[4:5]
	v_pk_mul_f32 v[62:63], v[10:11], v[10:11]
	v_pk_mul_f32 v[64:65], v[12:13], v[12:13]
	v_add_f32_e32 v58, v62, v63
	v_add_f32_e32 v58, v58, v64
	v_add_f32_e32 v58, v58, v65
	v_cvt_pk_f16_f32 v62, v10, v11
	v_cvt_pk_f16_f32 v63, v12, v13
	v_xor_b32_e32 v68, 0x60, v67
	ds_write_b64 v68, v[62:63]
	s_waitcnt vmcnt(0)
	v_cndmask_b32_e64 v6, v6, 0, s[2:3]
	v_cndmask_b32_e64 v7, v7, 0, s[2:3]
	v_cndmask_b32_e64 v8, v8, 0, s[2:3]
	v_cndmask_b32_e64 v9, v9, 0, s[2:3]
	v_pk_mul_f32 v[62:63], v[6:7], v[6:7]
	v_pk_mul_f32 v[64:65], v[8:9], v[8:9]
	v_add_f32_e32 v59, v62, v63
	v_add_f32_e32 v59, v59, v64
	v_add_f32_e32 v59, v59, v65
	v_cvt_pk_f16_f32 v62, v6, v7
	v_cvt_pk_f16_f32 v63, v8, v9
	v_xor_b32_e32 v68, 0x70, v67
	ds_write_b64 v68, v[62:63]
	v_add_f32_dpp v52, v52, v52 quad_perm:[1,0,3,2] row_mask:0xf bank_mask:0xf bound_ctrl:1
	v_add_f32_dpp v53, v53, v53 quad_perm:[1,0,3,2] row_mask:0xf bank_mask:0xf bound_ctrl:1
	v_add_f32_dpp v54, v54, v54 quad_perm:[1,0,3,2] row_mask:0xf bank_mask:0xf bound_ctrl:1
	v_add_f32_dpp v55, v55, v55 quad_perm:[1,0,3,2] row_mask:0xf bank_mask:0xf bound_ctrl:1
	v_add_f32_dpp v56, v56, v56 quad_perm:[1,0,3,2] row_mask:0xf bank_mask:0xf bound_ctrl:1
	v_add_f32_dpp v57, v57, v57 quad_perm:[1,0,3,2] row_mask:0xf bank_mask:0xf bound_ctrl:1
	v_add_f32_dpp v58, v58, v58 quad_perm:[1,0,3,2] row_mask:0xf bank_mask:0xf bound_ctrl:1
	v_add_f32_dpp v59, v59, v59 quad_perm:[1,0,3,2] row_mask:0xf bank_mask:0xf bound_ctrl:1
	v_add_f32_dpp v52, v52, v52 quad_perm:[2,3,0,1] row_mask:0xf bank_mask:0xf bound_ctrl:1
	v_add_f32_dpp v53, v53, v53 quad_perm:[2,3,0,1] row_mask:0xf bank_mask:0xf bound_ctrl:1
	v_add_f32_dpp v54, v54, v54 quad_perm:[2,3,0,1] row_mask:0xf bank_mask:0xf bound_ctrl:1
	v_add_f32_dpp v55, v55, v55 quad_perm:[2,3,0,1] row_mask:0xf bank_mask:0xf bound_ctrl:1
	v_add_f32_dpp v56, v56, v56 quad_perm:[2,3,0,1] row_mask:0xf bank_mask:0xf bound_ctrl:1
	v_add_f32_dpp v57, v57, v57 quad_perm:[2,3,0,1] row_mask:0xf bank_mask:0xf bound_ctrl:1
	v_add_f32_dpp v58, v58, v58 quad_perm:[2,3,0,1] row_mask:0xf bank_mask:0xf bound_ctrl:1
	v_add_f32_dpp v59, v59, v59 quad_perm:[2,3,0,1] row_mask:0xf bank_mask:0xf bound_ctrl:1
	v_add_f32_dpp v52, v52, v52 row_half_mirror row_mask:0xf bank_mask:0xf bound_ctrl:1
	v_add_f32_dpp v53, v53, v53 row_half_mirror row_mask:0xf bank_mask:0xf bound_ctrl:1
	v_add_f32_dpp v54, v54, v54 row_half_mirror row_mask:0xf bank_mask:0xf bound_ctrl:1
	v_add_f32_dpp v55, v55, v55 row_half_mirror row_mask:0xf bank_mask:0xf bound_ctrl:1
	v_add_f32_dpp v56, v56, v56 row_half_mirror row_mask:0xf bank_mask:0xf bound_ctrl:1
	v_add_f32_dpp v57, v57, v57 row_half_mirror row_mask:0xf bank_mask:0xf bound_ctrl:1
	v_add_f32_dpp v58, v58, v58 row_half_mirror row_mask:0xf bank_mask:0xf bound_ctrl:1
	v_add_f32_dpp v59, v59, v59 row_half_mirror row_mask:0xf bank_mask:0xf bound_ctrl:1
	v_add_f32_dpp v52, v52, v52 row_mirror row_mask:0xf bank_mask:0xf bound_ctrl:1
	v_add_f32_dpp v53, v53, v53 row_mirror row_mask:0xf bank_mask:0xf bound_ctrl:1
	v_add_f32_dpp v54, v54, v54 row_mirror row_mask:0xf bank_mask:0xf bound_ctrl:1
	v_add_f32_dpp v55, v55, v55 row_mirror row_mask:0xf bank_mask:0xf bound_ctrl:1
	v_add_f32_dpp v56, v56, v56 row_mirror row_mask:0xf bank_mask:0xf bound_ctrl:1
	v_add_f32_dpp v57, v57, v57 row_mirror row_mask:0xf bank_mask:0xf bound_ctrl:1
	v_add_f32_dpp v58, v58, v58 row_mirror row_mask:0xf bank_mask:0xf bound_ctrl:1
	v_add_f32_dpp v59, v59, v59 row_mirror row_mask:0xf bank_mask:0xf bound_ctrl:1
	v_add_f32_dpp v52, v52, v52 row_bcast:15 row_mask:0xa bank_mask:0xf
	v_add_f32_dpp v53, v53, v53 row_bcast:15 row_mask:0xa bank_mask:0xf
	v_add_f32_dpp v54, v54, v54 row_bcast:15 row_mask:0xa bank_mask:0xf
	v_add_f32_dpp v55, v55, v55 row_bcast:15 row_mask:0xa bank_mask:0xf
	v_add_f32_dpp v56, v56, v56 row_bcast:15 row_mask:0xa bank_mask:0xf
	v_add_f32_dpp v57, v57, v57 row_bcast:15 row_mask:0xa bank_mask:0xf
	v_add_f32_dpp v58, v58, v58 row_bcast:15 row_mask:0xa bank_mask:0xf
	v_add_f32_dpp v59, v59, v59 row_bcast:15 row_mask:0xa bank_mask:0xf
	v_add_f32_dpp v52, v52, v52 row_bcast:31 row_mask:0xc bank_mask:0xf
	v_add_f32_dpp v53, v53, v53 row_bcast:31 row_mask:0xc bank_mask:0xf
	v_add_f32_dpp v54, v54, v54 row_bcast:31 row_mask:0xc bank_mask:0xf
	v_add_f32_dpp v55, v55, v55 row_bcast:31 row_mask:0xc bank_mask:0xf
	v_add_f32_dpp v56, v56, v56 row_bcast:31 row_mask:0xc bank_mask:0xf
	v_add_f32_dpp v57, v57, v57 row_bcast:31 row_mask:0xc bank_mask:0xf
	v_add_f32_dpp v58, v58, v58 row_bcast:31 row_mask:0xc bank_mask:0xf
	v_add_f32_dpp v59, v59, v59 row_bcast:31 row_mask:0xc bank_mask:0xf
	v_pk_add_f32 v[0:1], v[48:49], 0 op_sel_hi:[1,0]
	v_pk_add_f32 v[2:3], v[50:51], 0 op_sel_hi:[1,0]
	v_pk_add_f32 v[0:1], v[0:1], v[34:35]
	v_pk_add_f32 v[2:3], v[2:3], v[36:37]
	v_pk_add_f32 v[0:1], v[0:1], v[30:31]
	v_pk_add_f32 v[2:3], v[2:3], v[32:33]
	v_pk_add_f32 v[0:1], v[0:1], v[26:27]
	v_pk_add_f32 v[2:3], v[2:3], v[28:29]
	v_pk_add_f32 v[0:1], v[0:1], v[22:23]
	v_pk_add_f32 v[2:3], v[2:3], v[24:25]
	v_pk_add_f32 v[0:1], v[0:1], v[18:19]
	v_pk_add_f32 v[2:3], v[2:3], v[20:21]
	v_pk_add_f32 v[0:1], v[0:1], v[10:11]
	v_pk_add_f32 v[2:3], v[2:3], v[12:13]
	v_pk_add_f32 v[0:1], v[0:1], v[6:7]
	v_pk_add_f32 v[2:3], v[2:3], v[8:9]
	s_mov_b64 s[24:25], exec
	s_mov_b32 exec_lo, 0
	s_brev_b32 exec_hi, 1
	v_cndmask_b32_e64 v52, v52, v66, s[16:17]
	v_cndmask_b32_e64 v53, v53, v66, s[14:15]
	v_cndmask_b32_e64 v54, v54, v66, s[12:13]
	v_cndmask_b32_e64 v55, v55, v66, s[10:11]
	v_cndmask_b32_e64 v56, v56, v66, s[8:9]
	v_cndmask_b32_e64 v57, v57, v66, s[6:7]
	v_cndmask_b32_e64 v58, v58, v66, s[4:5]
	v_cndmask_b32_e64 v59, v59, v66, s[2:3]
	v_lshlrev_b32_e32 v61, 2, v39
	global_store_dwordx4 v61, v[52:55], s[22:23] sc1
	global_store_dwordx4 v61, v[56:59], s[22:23] offset:16 sc1
	s_mov_b64 exec, s[24:25]
	s_load_dwordx2 s[6:7], s[0:1], 0x18
	v_lshl_or_b32 v4, v44, 10, v40
	ds_write_b128 v4, v[0:3] offset:16384
	s_waitcnt lgkmcnt(0)
	s_barrier
	v_lshrrev_b32_e32 v12, 5, v38
	v_and_b32_e32 v12, 0x70, v12
	v_xor_b32_e32 v12, v38, v12
	ds_read_b128 v[0:3], v12
	ds_read_b128 v[4:7], v12 offset:4096
	v_mov_b32_e32 v39, 0
	v_lshl_add_u64 v[8:9], s[18:19], 0, v[38:39]
	s_movk_i32 s0, 0x2000
	s_waitcnt lgkmcnt(1)
	global_store_dwordx4 v38, v[0:3], s[18:19] sc1
	ds_read_b128 v[0:3], v12 offset:8192
	v_add_co_u32_e32 v10, vcc, s0, v8
	s_movk_i32 s0, 0x3000
	s_nop 0
	v_addc_co_u32_e32 v11, vcc, 0, v9, vcc
	s_waitcnt lgkmcnt(1)
	global_store_dwordx4 v[10:11], v[4:7], off offset:-4096 sc1
	ds_read_b128 v[4:7], v12 offset:12288
	s_waitcnt lgkmcnt(1)
	global_store_dwordx4 v[10:11], v[0:3], off sc1
	ds_read2st64_b32 v[0:1], v45 offset0:64 offset1:68
	ds_read2st64_b32 v[2:3], v45 offset0:72 offset1:76
	v_add_co_u32_e32 v8, vcc, s0, v8
	s_lshl_b64 s[0:1], s[20:21], 10
	s_waitcnt lgkmcnt(1)
	v_add_f32_e32 v0, v0, v1
	s_waitcnt lgkmcnt(0)
	v_add_f32_e32 v0, v0, v2
	s_add_u32 s0, s6, s0
	v_addc_co_u32_e32 v9, vcc, 0, v9, vcc
	v_add_f32_e32 v0, v0, v3
	s_addc_u32 s1, s7, s1
	global_store_dwordx4 v[8:9], v[4:7], off sc1
	global_store_dword v45, v0, s[0:1]
